# GEMM epilogue copy-out hand-written: 9 LDS reads in flight, select-based segment addressing, interleaved K-norm chains, direct ds_max instead of scalar lane loop
# speedup vs baseline: 1.0798x; 1.0259x over previous
.LBB1_154:
	s_load_dwordx4 s[12:15], s[0:1], 0x18
	s_load_dwordx4 s[20:23], s[0:1], 0x28
	v_and_b32_e32 v100, 7, v0
	v_lshrrev_b32_e32 v101, 3, v0
	v_mul_u32_u24_e32 v102, 0x90, v101
	v_lshl_add_u32 v102, v100, 4, v102
	v_add_u32_e32 v103, 0x2400, v102
	v_add_u32_e32 v104, 0x4800, v102
	v_lshlrev_b32_e32 v105, 4, v0
	v_add_u32_e32 v106, 0x2000, v105
	v_add_u32_e32 v107, 0x4000, v105
	s_movk_i32 s45, 0xffe8
	v_mov_b32_e32 v168, v0
	v_mul_u32_u24_e32 v169, 0xaab, v168
	v_lshrrev_b32_e32 v169, 16, v169
	v_mad_i32_i24 v170, v169, s45, v168
	v_mul_u32_u24_e32 v171, 0x190, v169
	v_lshl_add_u32 v108, v170, 4, v171
	v_mul_u32_u24_e32 v171, 0x1800, v169
	v_lshl_add_u32 v111, v170, 4, v171
	v_add_u32_e32 v168, 0x200, v0
	v_mul_u32_u24_e32 v169, 0xaab, v168
	v_lshrrev_b32_e32 v169, 16, v169
	v_mad_i32_i24 v170, v169, s45, v168
	v_mul_u32_u24_e32 v171, 0x190, v169
	v_lshl_add_u32 v109, v170, 4, v171
	v_mul_u32_u24_e32 v171, 0x1800, v169
	v_lshl_add_u32 v112, v170, 4, v171
	v_add_u32_e32 v168, 0x400, v0
	v_mul_u32_u24_e32 v169, 0xaab, v168
	v_lshrrev_b32_e32 v169, 16, v169
	v_mad_i32_i24 v170, v169, s45, v168
	v_mul_u32_u24_e32 v171, 0x190, v169
	v_lshl_add_u32 v110, v170, 4, v171
	v_mul_u32_u24_e32 v171, 0x1800, v169
	v_lshl_add_u32 v113, v170, 4, v171
	v_cmp_eq_u32_e64 s[46:47], 0, v100
	v_mov_b32_e32 v174, 0
	s_waitcnt vmcnt(0) lgkmcnt(0)
	s_barrier
	s_add_i32 s24, s10, 0x0
	s_lshr_b32 s42, s24, 10
	s_bfe_u32 s26, s24, 0x40006
	s_mul_i32 s27, s26, 0xc00
	s_add_i32 s27, s27, s16
	s_lshl_b32 s27, s27, 7
	s_mul_i32 s28, s26, 0x60000
	s_lshl_b32 s29, s16, 1
	s_add_i32 s28, s28, s29
	s_cmp_eq_u32 s42, 0
	s_cselect_b32 s30, s12, s14
	s_cselect_b32 s31, s13, s15
	s_cmp_gt_u32 s42, 1
	s_cselect_b32 s30, s20, s30
	s_cselect_b32 s31, s21, s31
	s_cselect_b32 s27, s28, s27
	s_cselect_b64 s[24:25], -1, 0
	s_add_u32 s36, s30, s27
	s_addc_u32 s37, s31, 0
	v_cndmask_b32_e64 v114, v102, v108, s[24:25]
	v_cndmask_b32_e64 v123, v105, v111, s[24:25]
	v_cndmask_b32_e64 v115, v103, v109, s[24:25]
	v_cndmask_b32_e64 v124, v106, v112, s[24:25]
	v_cndmask_b32_e64 v116, v104, v110, s[24:25]
	v_cndmask_b32_e64 v125, v107, v113, s[24:25]
	ds_read_b128 v[132:135], v114 offset:1024
	ds_read_b128 v[136:139], v115 offset:1024
	ds_read_b128 v[140:143], v116 offset:1024
	s_add_i32 s24, s10, 0x40
	s_lshr_b32 s43, s24, 10
	s_bfe_u32 s26, s24, 0x40006
	s_mul_i32 s27, s26, 0xc00
	s_add_i32 s27, s27, s16
	s_lshl_b32 s27, s27, 7
	s_mul_i32 s28, s26, 0x60000
	s_lshl_b32 s29, s16, 1
	s_add_i32 s28, s28, s29
	s_cmp_eq_u32 s43, 0
	s_cselect_b32 s30, s12, s14
	s_cselect_b32 s31, s13, s15
	s_cmp_gt_u32 s43, 1
	s_cselect_b32 s30, s20, s30
	s_cselect_b32 s31, s21, s31
	s_cselect_b32 s27, s28, s27
	s_cselect_b64 s[24:25], -1, 0
	s_add_u32 s38, s30, s27
	s_addc_u32 s39, s31, 0
	v_cndmask_b32_e64 v117, v102, v108, s[24:25]
	v_cndmask_b32_e64 v126, v105, v111, s[24:25]
	v_cndmask_b32_e64 v118, v103, v109, s[24:25]
	v_cndmask_b32_e64 v127, v106, v112, s[24:25]
	v_cndmask_b32_e64 v119, v104, v110, s[24:25]
	v_cndmask_b32_e64 v128, v107, v113, s[24:25]
	ds_read_b128 v[144:147], v117 offset:28672
	ds_read_b128 v[148:151], v118 offset:28672
	ds_read_b128 v[152:155], v119 offset:28672
	s_add_i32 s24, s10, 0x80
	s_lshr_b32 s44, s24, 10
	s_bfe_u32 s26, s24, 0x40006
	s_mul_i32 s27, s26, 0xc00
	s_add_i32 s27, s27, s16
	s_lshl_b32 s27, s27, 7
	s_mul_i32 s28, s26, 0x60000
	s_lshl_b32 s29, s16, 1
	s_add_i32 s28, s28, s29
	s_cmp_eq_u32 s44, 0
	s_cselect_b32 s30, s12, s14
	s_cselect_b32 s31, s13, s15
	s_cmp_gt_u32 s44, 1
	s_cselect_b32 s30, s20, s30
	s_cselect_b32 s31, s21, s31
	s_cselect_b32 s27, s28, s27
	s_cselect_b64 s[24:25], -1, 0
	s_add_u32 s40, s30, s27
	s_addc_u32 s41, s31, 0
	v_cndmask_b32_e64 v120, v102, v108, s[24:25]
	v_cndmask_b32_e64 v129, v105, v111, s[24:25]
	v_cndmask_b32_e64 v121, v103, v109, s[24:25]
	v_cndmask_b32_e64 v130, v106, v112, s[24:25]
	v_cndmask_b32_e64 v122, v104, v110, s[24:25]
	v_cndmask_b32_e64 v131, v107, v113, s[24:25]
	ds_read_b128 v[156:159], v120 offset:56320
	ds_read_b128 v[160:163], v121 offset:56320
	ds_read_b128 v[164:167], v122 offset:56320
	s_waitcnt lgkmcnt(8)
	global_store_dwordx4 v123, v[132:135], s[36:37] sc1
	s_waitcnt lgkmcnt(7)
	global_store_dwordx4 v124, v[136:139], s[36:37] sc1
	s_waitcnt lgkmcnt(6)
	global_store_dwordx4 v125, v[140:143], s[36:37] sc1
	s_waitcnt lgkmcnt(5)
	global_store_dwordx4 v126, v[144:147], s[38:39] sc1
	s_waitcnt lgkmcnt(4)
	global_store_dwordx4 v127, v[148:151], s[38:39] sc1
	s_waitcnt lgkmcnt(3)
	global_store_dwordx4 v128, v[152:155], s[38:39] sc1
	s_waitcnt lgkmcnt(2)
	global_store_dwordx4 v129, v[156:159], s[40:41] sc1
	s_waitcnt lgkmcnt(1)
	global_store_dwordx4 v130, v[160:163], s[40:41] sc1
	s_waitcnt lgkmcnt(0)
	global_store_dwordx4 v131, v[164:167], s[40:41] sc1
	s_cmp_lg_u32 s42, 1
	s_cbranch_scc1 .Lgemm_kn_skip0
	v_fma_mix_f32 v168, v132, v132, 0 op_sel_hi:[1,1,0]
	v_fma_mix_f32 v170, v136, v136, 0 op_sel_hi:[1,1,0]
	v_fma_mix_f32 v172, v140, v140, 0 op_sel_hi:[1,1,0]
	v_fma_mix_f32 v168, v132, v132, v168 op_sel:[1,1,0] op_sel_hi:[1,1,0]
	v_fma_mix_f32 v170, v136, v136, v170 op_sel:[1,1,0] op_sel_hi:[1,1,0]
	v_fma_mix_f32 v172, v140, v140, v172 op_sel:[1,1,0] op_sel_hi:[1,1,0]
	v_fma_mix_f32 v168, v133, v133, v168 op_sel_hi:[1,1,0]
	v_fma_mix_f32 v170, v137, v137, v170 op_sel_hi:[1,1,0]
	v_fma_mix_f32 v172, v141, v141, v172 op_sel_hi:[1,1,0]
	v_fma_mix_f32 v168, v133, v133, v168 op_sel:[1,1,0] op_sel_hi:[1,1,0]
	v_fma_mix_f32 v170, v137, v137, v170 op_sel:[1,1,0] op_sel_hi:[1,1,0]
	v_fma_mix_f32 v172, v141, v141, v172 op_sel:[1,1,0] op_sel_hi:[1,1,0]
	v_fma_mix_f32 v168, v134, v134, v168 op_sel_hi:[1,1,0]
	v_fma_mix_f32 v170, v138, v138, v170 op_sel_hi:[1,1,0]
	v_fma_mix_f32 v172, v142, v142, v172 op_sel_hi:[1,1,0]
	v_fma_mix_f32 v168, v134, v134, v168 op_sel:[1,1,0] op_sel_hi:[1,1,0]
	v_fma_mix_f32 v170, v138, v138, v170 op_sel:[1,1,0] op_sel_hi:[1,1,0]
	v_fma_mix_f32 v172, v142, v142, v172 op_sel:[1,1,0] op_sel_hi:[1,1,0]
	v_fma_mix_f32 v168, v135, v135, v168 op_sel_hi:[1,1,0]
	v_fma_mix_f32 v170, v139, v139, v170 op_sel_hi:[1,1,0]
	v_fma_mix_f32 v172, v143, v143, v172 op_sel_hi:[1,1,0]
	v_fma_mix_f32 v168, v135, v135, v168 op_sel:[1,1,0] op_sel_hi:[1,1,0]
	v_fma_mix_f32 v170, v139, v139, v170 op_sel:[1,1,0] op_sel_hi:[1,1,0]
	v_fma_mix_f32 v172, v143, v143, v172 op_sel:[1,1,0] op_sel_hi:[1,1,0]
	s_nop 1
	v_add_f32_dpp v168, v168, v168 quad_perm:[1,0,3,2] row_mask:0xf bank_mask:0xf bound_ctrl:1
	v_add_f32_dpp v170, v170, v170 quad_perm:[1,0,3,2] row_mask:0xf bank_mask:0xf bound_ctrl:1
	v_add_f32_dpp v172, v172, v172 quad_perm:[1,0,3,2] row_mask:0xf bank_mask:0xf bound_ctrl:1
	s_nop 0
	v_add_f32_dpp v168, v168, v168 quad_perm:[2,3,0,1] row_mask:0xf bank_mask:0xf bound_ctrl:1
	v_add_f32_dpp v170, v170, v170 quad_perm:[2,3,0,1] row_mask:0xf bank_mask:0xf bound_ctrl:1
	v_add_f32_dpp v172, v172, v172 quad_perm:[2,3,0,1] row_mask:0xf bank_mask:0xf bound_ctrl:1
	s_nop 0
	v_mov_b32_dpp v169, v168 row_half_mirror row_mask:0xf bank_mask:0xf bound_ctrl:1
	v_mov_b32_dpp v171, v170 row_half_mirror row_mask:0xf bank_mask:0xf bound_ctrl:1
	v_mov_b32_dpp v173, v172 row_half_mirror row_mask:0xf bank_mask:0xf bound_ctrl:1
	s_nop 0
	v_add_f32_e32 v168, v168, v169
	v_add_f32_e32 v170, v170, v171
	v_add_f32_e32 v172, v172, v173
	s_and_saveexec_b64 s[48:49], s[46:47]
	ds_max_u32 v174, v168
	ds_max_u32 v174, v170 offset:4
	ds_max_u32 v174, v172 offset:8
	s_mov_b64 exec, s[48:49]
.Lgemm_kn_skip0:
	s_cmp_lg_u32 s43, 1
	s_cbranch_scc1 .Lgemm_kn_skip1
	v_fma_mix_f32 v168, v144, v144, 0 op_sel_hi:[1,1,0]
	v_fma_mix_f32 v170, v148, v148, 0 op_sel_hi:[1,1,0]
	v_fma_mix_f32 v172, v152, v152, 0 op_sel_hi:[1,1,0]
	v_fma_mix_f32 v168, v144, v144, v168 op_sel:[1,1,0] op_sel_hi:[1,1,0]
	v_fma_mix_f32 v170, v148, v148, v170 op_sel:[1,1,0] op_sel_hi:[1,1,0]
	v_fma_mix_f32 v172, v152, v152, v172 op_sel:[1,1,0] op_sel_hi:[1,1,0]
	v_fma_mix_f32 v168, v145, v145, v168 op_sel_hi:[1,1,0]
	v_fma_mix_f32 v170, v149, v149, v170 op_sel_hi:[1,1,0]
	v_fma_mix_f32 v172, v153, v153, v172 op_sel_hi:[1,1,0]
	v_fma_mix_f32 v168, v145, v145, v168 op_sel:[1,1,0] op_sel_hi:[1,1,0]
	v_fma_mix_f32 v170, v149, v149, v170 op_sel:[1,1,0] op_sel_hi:[1,1,0]
	v_fma_mix_f32 v172, v153, v153, v172 op_sel:[1,1,0] op_sel_hi:[1,1,0]
	v_fma_mix_f32 v168, v146, v146, v168 op_sel_hi:[1,1,0]
	v_fma_mix_f32 v170, v150, v150, v170 op_sel_hi:[1,1,0]
	v_fma_mix_f32 v172, v154, v154, v172 op_sel_hi:[1,1,0]
	v_fma_mix_f32 v168, v146, v146, v168 op_sel:[1,1,0] op_sel_hi:[1,1,0]
	v_fma_mix_f32 v170, v150, v150, v170 op_sel:[1,1,0] op_sel_hi:[1,1,0]
	v_fma_mix_f32 v172, v154, v154, v172 op_sel:[1,1,0] op_sel_hi:[1,1,0]
	v_fma_mix_f32 v168, v147, v147, v168 op_sel_hi:[1,1,0]
	v_fma_mix_f32 v170, v151, v151, v170 op_sel_hi:[1,1,0]
	v_fma_mix_f32 v172, v155, v155, v172 op_sel_hi:[1,1,0]
	v_fma_mix_f32 v168, v147, v147, v168 op_sel:[1,1,0] op_sel_hi:[1,1,0]
	v_fma_mix_f32 v170, v151, v151, v170 op_sel:[1,1,0] op_sel_hi:[1,1,0]
	v_fma_mix_f32 v172, v155, v155, v172 op_sel:[1,1,0] op_sel_hi:[1,1,0]
	s_nop 1
	v_add_f32_dpp v168, v168, v168 quad_perm:[1,0,3,2] row_mask:0xf bank_mask:0xf bound_ctrl:1
	v_add_f32_dpp v170, v170, v170 quad_perm:[1,0,3,2] row_mask:0xf bank_mask:0xf bound_ctrl:1
	v_add_f32_dpp v172, v172, v172 quad_perm:[1,0,3,2] row_mask:0xf bank_mask:0xf bound_ctrl:1
	s_nop 0
	v_add_f32_dpp v168, v168, v168 quad_perm:[2,3,0,1] row_mask:0xf bank_mask:0xf bound_ctrl:1
	v_add_f32_dpp v170, v170, v170 quad_perm:[2,3,0,1] row_mask:0xf bank_mask:0xf bound_ctrl:1
	v_add_f32_dpp v172, v172, v172 quad_perm:[2,3,0,1] row_mask:0xf bank_mask:0xf bound_ctrl:1
	s_nop 0
	v_mov_b32_dpp v169, v168 row_half_mirror row_mask:0xf bank_mask:0xf bound_ctrl:1
	v_mov_b32_dpp v171, v170 row_half_mirror row_mask:0xf bank_mask:0xf bound_ctrl:1
	v_mov_b32_dpp v173, v172 row_half_mirror row_mask:0xf bank_mask:0xf bound_ctrl:1
	s_nop 0
	v_add_f32_e32 v168, v168, v169
	v_add_f32_e32 v170, v170, v171
	v_add_f32_e32 v172, v172, v173
	s_and_saveexec_b64 s[48:49], s[46:47]
	ds_max_u32 v174, v168 offset:12
	ds_max_u32 v174, v170 offset:16
	ds_max_u32 v174, v172 offset:20
	s_mov_b64 exec, s[48:49]
.Lgemm_kn_skip1:
	s_cmp_lg_u32 s44, 1
	s_cbranch_scc1 .Lgemm_kn_skip2
	v_fma_mix_f32 v168, v156, v156, 0 op_sel_hi:[1,1,0]
	v_fma_mix_f32 v170, v160, v160, 0 op_sel_hi:[1,1,0]
	v_fma_mix_f32 v172, v164, v164, 0 op_sel_hi:[1,1,0]
	v_fma_mix_f32 v168, v156, v156, v168 op_sel:[1,1,0] op_sel_hi:[1,1,0]
	v_fma_mix_f32 v170, v160, v160, v170 op_sel:[1,1,0] op_sel_hi:[1,1,0]
	v_fma_mix_f32 v172, v164, v164, v172 op_sel:[1,1,0] op_sel_hi:[1,1,0]
	v_fma_mix_f32 v168, v157, v157, v168 op_sel_hi:[1,1,0]
	v_fma_mix_f32 v170, v161, v161, v170 op_sel_hi:[1,1,0]
	v_fma_mix_f32 v172, v165, v165, v172 op_sel_hi:[1,1,0]
	v_fma_mix_f32 v168, v157, v157, v168 op_sel:[1,1,0] op_sel_hi:[1,1,0]
	v_fma_mix_f32 v170, v161, v161, v170 op_sel:[1,1,0] op_sel_hi:[1,1,0]
	v_fma_mix_f32 v172, v165, v165, v172 op_sel:[1,1,0] op_sel_hi:[1,1,0]
	v_fma_mix_f32 v168, v158, v158, v168 op_sel_hi:[1,1,0]
	v_fma_mix_f32 v170, v162, v162, v170 op_sel_hi:[1,1,0]
	v_fma_mix_f32 v172, v166, v166, v172 op_sel_hi:[1,1,0]
	v_fma_mix_f32 v168, v158, v158, v168 op_sel:[1,1,0] op_sel_hi:[1,1,0]
	v_fma_mix_f32 v170, v162, v162, v170 op_sel:[1,1,0] op_sel_hi:[1,1,0]
	v_fma_mix_f32 v172, v166, v166, v172 op_sel:[1,1,0] op_sel_hi:[1,1,0]
	v_fma_mix_f32 v168, v159, v159, v168 op_sel_hi:[1,1,0]
	v_fma_mix_f32 v170, v163, v163, v170 op_sel_hi:[1,1,0]
	v_fma_mix_f32 v172, v167, v167, v172 op_sel_hi:[1,1,0]
	v_fma_mix_f32 v168, v159, v159, v168 op_sel:[1,1,0] op_sel_hi:[1,1,0]
	v_fma_mix_f32 v170, v163, v163, v170 op_sel:[1,1,0] op_sel_hi:[1,1,0]
	v_fma_mix_f32 v172, v167, v167, v172 op_sel:[1,1,0] op_sel_hi:[1,1,0]
	s_nop 1
	v_add_f32_dpp v168, v168, v168 quad_perm:[1,0,3,2] row_mask:0xf bank_mask:0xf bound_ctrl:1
	v_add_f32_dpp v170, v170, v170 quad_perm:[1,0,3,2] row_mask:0xf bank_mask:0xf bound_ctrl:1
	v_add_f32_dpp v172, v172, v172 quad_perm:[1,0,3,2] row_mask:0xf bank_mask:0xf bound_ctrl:1
	s_nop 0
	v_add_f32_dpp v168, v168, v168 quad_perm:[2,3,0,1] row_mask:0xf bank_mask:0xf bound_ctrl:1
	v_add_f32_dpp v170, v170, v170 quad_perm:[2,3,0,1] row_mask:0xf bank_mask:0xf bound_ctrl:1
	v_add_f32_dpp v172, v172, v172 quad_perm:[2,3,0,1] row_mask:0xf bank_mask:0xf bound_ctrl:1
	s_nop 0
	v_mov_b32_dpp v169, v168 row_half_mirror row_mask:0xf bank_mask:0xf bound_ctrl:1
	v_mov_b32_dpp v171, v170 row_half_mirror row_mask:0xf bank_mask:0xf bound_ctrl:1
	v_mov_b32_dpp v173, v172 row_half_mirror row_mask:0xf bank_mask:0xf bound_ctrl:1
	s_nop 0
	v_add_f32_e32 v168, v168, v169
	v_add_f32_e32 v170, v170, v171
	v_add_f32_e32 v172, v172, v173
	s_and_saveexec_b64 s[48:49], s[46:47]
	ds_max_u32 v174, v168 offset:24
	ds_max_u32 v174, v170 offset:28
	ds_max_u32 v174, v172 offset:32
	s_mov_b64 exec, s[48:49]
.Lgemm_kn_skip2:
	v_cmp_gt_u32_e64 s[4:5], 9, v0
.LBB1_226:
	s_waitcnt lgkmcnt(0)
	s_barrier
	s_and_saveexec_b64 s[6:7], s[4:5]
	s_cbranch_execz .LBB1_229
	v_mul_lo_u16_e32 v1, 0xab, v0
	v_lshrrev_b16_e32 v1, 9, v1
	v_lshl_add_u32 v2, v1, 6, s10
	v_and_b32_e32 v3, 0xfffffc00, v2
	s_movk_i32 s2, 0x400
	v_cmp_eq_u32_e32 vcc, s2, v3
	s_and_b64 exec, exec, vcc
	s_cbranch_execz .LBB1_229
	s_load_dwordx2 s[0:1], s[0:1], 0x30
	v_mad_i32_i24 v4, v1, -3, v0
	v_bfe_u32 v1, v2, 6, 4
	v_mul_u32_u24_e32 v1, 48, v1
	v_lshlrev_b32_e32 v0, 2, v0
	v_lshlrev_b32_e32 v2, 2, v1
	v_mov_b32_e32 v3, 0
	ds_read_b32 v6, v0
	s_waitcnt lgkmcnt(0)
	v_lshl_add_u64 v[2:3], s[0:1], 0, v[2:3]
	s_mul_i32 s0, s3, 3
	s_ashr_i32 s1, s0, 31
	v_lshl_add_u64 v[0:1], s[0:1], 2, v[2:3]
	v_ashrrev_i32_e32 v5, 31, v4
	v_lshl_add_u64 v[0:1], v[4:5], 2, v[0:1]
	global_atomic_umax v[0:1], v6, off

	.amdhsa_kernel _Z8gemm_qkvPKDF16_S0_PKfPDF16_S3_S3_Pj
		.amdhsa_group_segment_fixed_size 1024
		.amdhsa_private_segment_fixed_size 0
		.amdhsa_kernarg_size 56
		.amdhsa_user_sgpr_count 2
		.amdhsa_user_sgpr_dispatch_ptr 0
		.amdhsa_user_sgpr_queue_ptr 0
		.amdhsa_user_sgpr_kernarg_segment_ptr 1
		.amdhsa_user_sgpr_dispatch_id 0
		.amdhsa_user_sgpr_kernarg_preload_length 0
		.amdhsa_user_sgpr_kernarg_preload_offset 0
		.amdhsa_user_sgpr_private_segment_size 0
		.amdhsa_uses_dynamic_stack 0
		.amdhsa_enable_private_segment 0
		.amdhsa_system_sgpr_workgroup_id_x 1
		.amdhsa_system_sgpr_workgroup_id_y 1
		.amdhsa_system_sgpr_workgroup_id_z 0
		.amdhsa_system_sgpr_workgroup_info 0
		.amdhsa_system_vgpr_workitem_id 0
		.amdhsa_next_free_vgpr 256
		.amdhsa_next_free_sgpr 56
		.amdhsa_accum_offset 256
		.amdhsa_reserve_vcc 1
		.amdhsa_float_round_mode_32 0
		.amdhsa_float_round_mode_16_64 0
		.amdhsa_float_denorm_mode_32 3
		.amdhsa_float_denorm_mode_16_64 3
		.amdhsa_dx10_clamp 1
		.amdhsa_ieee_mode 1
		.amdhsa_fp16_overflow 0
		.amdhsa_tg_split 0
		.amdhsa_exception_fp_ieee_invalid_op 0
		.amdhsa_exception_fp_denorm_src 0
		.amdhsa_exception_fp_ieee_div_zero 0
		.amdhsa_exception_fp_ieee_overflow 0
		.amdhsa_exception_fp_ieee_underflow 0
		.amdhsa_exception_fp_ieee_inexact 0
		.amdhsa_exception_int_div_zero 0
	.end_amdhsa_kernel

amdhsa.kernels:
  - .agpr_count:     0
    .args:
      - .actual_access:  read_only
        .address_space:  global
        .offset:         0
        .size:           8
        .value_kind:     global_buffer
      - .actual_access:  read_only
        .address_space:  global
        .offset:         8
        .size:           8
        .value_kind:     global_buffer
      - .address_space:  global
        .offset:         16
        .size:           8
        .value_kind:     global_buffer
      - .address_space:  global
        .offset:         24
        .size:           8
        .value_kind:     global_buffer
      - .offset:         32
        .size:           4
        .value_kind:     by_value
      - .actual_access:  write_only
        .address_space:  global
        .offset:         40
        .size:           8
        .value_kind:     global_buffer
    .group_segment_fixed_size: 0
    .kernarg_segment_align: 8
    .kernarg_segment_size: 48
    .language:       OpenCL C
    .language_version:
      - 2
      - 0
    .max_flat_workgroup_size: 256
    .name:           _Z7cvt_f16PKfS0_PDF16_S1_iPj
    .private_segment_fixed_size: 0
    .sgpr_count:     32
    .sgpr_spill_count: 0
    .symbol:         _Z7cvt_f16PKfS0_PDF16_S1_iPj.kd
    .uniform_work_group_size: 1
    .uses_dynamic_stack: false
    .vgpr_count:     50
    .vgpr_spill_count: 0
    .wavefront_size: 64
  - .agpr_count:     0
    .args:
      - .address_space:  global
        .offset:         0
        .size:           8
        .value_kind:     global_buffer
      - .address_space:  global
        .offset:         8
        .size:           8
        .value_kind:     global_buffer
      - .actual_access:  read_only
        .address_space:  global
        .offset:         16
        .size:           8
        .value_kind:     global_buffer
      - .address_space:  global
        .offset:         24
        .size:           8
        .value_kind:     global_buffer
      - .address_space:  global
        .offset:         32
        .size:           8
        .value_kind:     global_buffer
      - .address_space:  global
        .offset:         40
        .size:           8
        .value_kind:     global_buffer
      - .address_space:  global
        .offset:         48
        .size:           8
        .value_kind:     global_buffer
    .group_segment_fixed_size: 1024
    .kernarg_segment_align: 8
    .kernarg_segment_size: 56
    .language:       OpenCL C
    .language_version:
      - 2
      - 0
    .max_flat_workgroup_size: 512
    .name:           _Z8gemm_qkvPKDF16_S0_PKfPDF16_S3_S3_Pj
    .private_segment_fixed_size: 0
    .sgpr_count:     62
    .sgpr_spill_count: 0
    .symbol:         _Z8gemm_qkvPKDF16_S0_PKfPDF16_S3_S3_Pj.kd
    .uniform_work_group_size: 1
    .uses_dynamic_stack: false
    .vgpr_count:     256
    .vgpr_spill_count: 0
    .wavefront_size: 64
  - .agpr_count:     0
    .args:
      - .actual_access:  read_only
        .address_space:  global
        .offset:         0
        .size:           8
        .value_kind:     global_buffer
      - .address_space:  global
        .offset:         8
        .size:           8
        .value_kind:     global_buffer
      - .address_space:  global
        .offset:         16
        .size:           8
        .value_kind:     global_buffer
      - .actual_access:  read_only
        .address_space:  global
        .offset:         24
        .size:           8
        .value_kind:     global_buffer
      - .address_space:  global
        .offset:         32
        .size:           8
        .value_kind:     global_buffer
    .group_segment_fixed_size: 132896
    .kernarg_segment_align: 8
    .kernarg_segment_size: 40
    .language:       OpenCL C
    .language_version:
      - 2
      - 0
    .max_flat_workgroup_size: 512
    .name:           _Z8attn_fwdPKDF16_S0_S0_PKjPf
    .private_segment_fixed_size: 0
    .sgpr_count:     41
    .sgpr_spill_count: 0
    .symbol:         _Z8attn_fwdPKDF16_S0_S0_PKjPf.kd
    .uniform_work_group_size: 1
    .uses_dynamic_stack: false
    .vgpr_count:     242
    .vgpr_spill_count: 0
    .wavefront_size: 64
